# out-projection skinny epilogue: residual piece requested before the cross-wave reduction instead of after it
# speedup vs baseline: 1.0016x; 1.0016x over previous
; template <class Epi>
; DI void skinny64(const bf16* A, int lda, const bf16* Bt, int ldb, int N, int K, int r0, LAS unsigned char* lds, const Epi& epi, int wave, int lane, int bid, int G) {
;     ...
;         if (wave < 2) { f32x4 s = red[wave * 64 + lane];
; #pragma unroll
;             for (int w = 1; w < 8; ++w) s = s + red[(w * 2 + wave) * 64 + lane];
;             epi(r0 + 32 * mh + 16 * wave + n16, 16 * nt + 4 * q, s); }
.LBB0_1572:
	v_or_b32_e32 v198, s33, v49
	v_lshlrev_b64 v[200:201], 13, v[40:41]
	v_ashrrev_i32_e32 v199, 31, v198
	v_lshl_add_u64 v[200:201], v[42:43], 0, v[200:201]
	v_lshlrev_b64 v[202:203], 2, v[198:199]
	v_lshl_add_u64 v[200:201], v[200:201], 0, v[202:203]
	global_load_dwordx4 v[204:207], v[200:201], off
	s_waitcnt lgkmcnt(6)
	v_pk_add_f32 v[22:23], v[22:23], v[30:31]
	v_pk_add_f32 v[24:25], v[24:25], v[32:33]
	s_waitcnt lgkmcnt(5)
	v_pk_add_f32 v[22:23], v[22:23], v[26:27]
	v_pk_add_f32 v[24:25], v[24:25], v[28:29]
	s_waitcnt lgkmcnt(4)
	v_pk_add_f32 v[18:19], v[22:23], v[18:19]
	v_pk_add_f32 v[20:21], v[24:25], v[20:21]
	s_waitcnt lgkmcnt(3)
	v_pk_add_f32 v[14:15], v[18:19], v[14:15]
	v_pk_add_f32 v[16:17], v[20:21], v[16:17]
	s_waitcnt lgkmcnt(2)
	v_pk_add_f32 v[10:11], v[14:15], v[10:11]
	v_pk_add_f32 v[12:13], v[16:17], v[12:13]
	s_waitcnt lgkmcnt(1)
	v_pk_add_f32 v[6:7], v[10:11], v[6:7]
	v_pk_add_f32 v[8:9], v[12:13], v[8:9]
	s_waitcnt lgkmcnt(0)
	v_pk_add_f32 v[6:7], v[6:7], v[2:3]
	v_pk_add_f32 v[8:9], v[8:9], v[4:5]
	s_waitcnt vmcnt(0)
	v_pk_add_f32 v[2:3], v[6:7], v[204:205]
	v_lshlrev_b64 v[6:7], 13, v[38:39]
	v_lshl_add_u64 v[6:7], s[8:9], 0, v[6:7]
	v_pk_add_f32 v[4:5], v[8:9], v[206:207]
	v_lshl_add_u64 v[6:7], v[6:7], 0, v[202:203]
	global_store_dwordx4 v[6:7], v[2:5], off
